# grid barrier: waiters poll the TOP arrival counter directly (no TOPGEN/XGEN relay hops), early acquire invalidate
# speedup vs baseline: 1.0096x; 1.0096x over previous
.LBB0_234:
	v_readlane_b32 s4, v253, 25
	s_lshl_b32 s4, s4, 8
	v_readlane_b32 s6, v253, 21
	v_readlane_b32 s7, v253, 22
	s_add_u32 s4, s6, s4
	s_addc_u32 s5, s7, 0
	v_mov_b32_e32 v1, 0x1000
	v_mov_b32_e32 v3, 1
	global_atomic_add v3, v1, v3, s[4:5] offset:1024 sc0
	buffer_inv sc1
	v_cvt_f32_u32_e32 v1, v2
	v_sub_u32_e32 v4, 0, v2
	s_add_u32 s4, s4, 0x2400
	s_addc_u32 s5, s5, 0
	v_rcp_iflag_f32_e32 v1, v1
	s_nop 0
	v_mul_f32_e32 v1, 0x4f7ffffe, v1
	v_cvt_u32_f32_e32 v1, v1
	v_mul_lo_u32 v4, v4, v1
	v_mul_hi_u32 v4, v1, v4
	v_add_u32_e32 v1, v1, v4
	s_waitcnt vmcnt(1)
	v_mul_hi_u32 v1, v3, v1
	v_mul_lo_u32 v4, v1, v2
	v_sub_u32_e32 v4, v3, v4
	v_add_u32_e32 v5, 1, v1
	v_cmp_ge_u32_e32 vcc, v4, v2
	v_add_u32_e32 v3, 1, v3
	s_nop 0
	v_cndmask_b32_e32 v1, v1, v5, vcc
	v_sub_u32_e32 v5, v4, v2
	v_cndmask_b32_e32 v4, v4, v5, vcc
	v_add_u32_e32 v5, 1, v1
	v_cmp_ge_u32_e32 vcc, v4, v2
	s_nop 1
	v_cndmask_b32_e32 v1, v1, v5, vcc
	v_mul_lo_u32 v4, v2, v1
	v_add_u32_e32 v2, v4, v2
	v_cmp_ne_u32_e32 vcc, v3, v2
	s_cbranch_vccz .Lxb_lead_0
	v_mad_u32_u24 v2, v1, v0, v0
	v_mov_b32_e32 v0, 0x7000
.Lxb_poll_0:
	global_load_dword v3, v0, s[94:95] offset:1024 sc1
	s_waitcnt vmcnt(0)
	v_cmp_lt_u32_e32 vcc, v3, v2
	s_cbranch_vccz .Lxb_end_0
	s_sleep 1
	s_branch .Lxb_poll_0
.Lxb_lead_0:
	buffer_wbl2 sc1
	v_mad_u32_u24 v2, v1, v0, v0
	v_mov_b32_e32 v0, 0x7000
	v_mov_b32_e32 v3, 1
	s_waitcnt vmcnt(0) lgkmcnt(0)
	global_atomic_add v3, v0, v3, s[94:95] offset:1024 sc0
	s_waitcnt vmcnt(0)
	v_add_u32_e32 v3, 1, v3
.Lxb_lpoll_0:
	v_cmp_lt_u32_e32 vcc, v3, v2
	s_cbranch_vccz .Lxb_end_0
	s_sleep 1
	global_load_dword v3, v0, s[94:95] offset:1024 sc1
	s_waitcnt vmcnt(0)
	s_branch .Lxb_lpoll_0
.Lxb_end_0:
	s_waitcnt vmcnt(0)
.LBB0_266:
	s_or_b64 exec, exec, s[0:1]
	v_readlane_b32 s6, v253, 23
	v_readlane_b32 s7, v253, 24
	s_waitcnt lgkmcnt(0)
	s_barrier

.LBB0_315:
	v_readlane_b32 s2, v253, 25
	s_lshl_b32 s2, s2, 8
	v_readlane_b32 s4, v253, 21
	v_readlane_b32 s5, v253, 22
	s_add_u32 s2, s4, s2
	s_addc_u32 s3, s5, 0
	v_mov_b32_e32 v1, 0x1000
	v_mov_b32_e32 v3, 1
	global_atomic_add v3, v1, v3, s[2:3] offset:1024 sc0
	buffer_inv sc1
	v_cvt_f32_u32_e32 v1, v2
	v_sub_u32_e32 v4, 0, v2
	v_rcp_iflag_f32_e32 v1, v1
	s_nop 0
	v_mul_f32_e32 v1, 0x4f7ffffe, v1
	v_cvt_u32_f32_e32 v1, v1
	v_mul_lo_u32 v4, v4, v1
	v_mul_hi_u32 v4, v1, v4
	v_add_u32_e32 v1, v1, v4
	s_waitcnt vmcnt(1)
	v_mul_hi_u32 v1, v3, v1
	v_mul_lo_u32 v4, v1, v2
	v_sub_u32_e32 v4, v3, v4
	v_add_u32_e32 v5, 1, v1
	v_cmp_ge_u32_e32 vcc, v4, v2
	v_add_u32_e32 v3, 1, v3
	s_nop 0
	v_cndmask_b32_e32 v1, v1, v5, vcc
	v_sub_u32_e32 v5, v4, v2
	v_cndmask_b32_e32 v4, v4, v5, vcc
	v_add_u32_e32 v5, 1, v1
	v_cmp_ge_u32_e32 vcc, v4, v2
	s_nop 1
	v_cndmask_b32_e32 v1, v1, v5, vcc
	v_mul_lo_u32 v4, v2, v1
	v_add_u32_e32 v2, v4, v2
	v_cmp_ne_u32_e32 vcc, v3, v2
	s_cbranch_vccz .Lxb_lead_1
	v_mad_u32_u24 v2, v1, v0, v0
	v_mov_b32_e32 v0, 0x7000

.Lxb_end_1:
	s_waitcnt vmcnt(0)
.LBB0_347:
	s_or_b64 exec, exec, s[0:1]
	v_readlane_b32 s6, v253, 23
	v_readlane_b32 s7, v253, 24
	s_waitcnt lgkmcnt(0)
	s_barrier

.Lxb_end_2:
	s_waitcnt vmcnt(0)
.LBB0_427:
	s_or_b64 exec, exec, s[0:1]
	v_readlane_b32 s6, v253, 23
	v_readlane_b32 s7, v253, 24
	s_waitcnt lgkmcnt(0)
	s_barrier

.Lxb_end_3:
	s_waitcnt vmcnt(0)
.LBB0_544:
	s_or_b64 exec, exec, s[0:1]
	v_readlane_b32 s6, v253, 23
	v_readlane_b32 s7, v253, 24
	s_waitcnt lgkmcnt(0)
	s_barrier

.Lxb_end_4:
	s_waitcnt vmcnt(0)
.LBB0_621:
	s_or_b64 exec, exec, s[0:1]
	v_readlane_b32 s6, v253, 23
	v_readlane_b32 s7, v253, 24
	s_waitcnt lgkmcnt(0)
	s_barrier

.Lxb_end_5:
	s_waitcnt vmcnt(0)
.LBB0_738:
	s_or_b64 exec, exec, s[0:1]
	v_readlane_b32 s6, v253, 23
	v_readlane_b32 s7, v253, 24
	s_waitcnt lgkmcnt(0)
	s_barrier

.Lxb_end_6:
	s_waitcnt vmcnt(0)
.LBB0_903:
	s_or_b64 exec, exec, s[0:1]
	v_readlane_b32 s6, v253, 23
	v_readlane_b32 s7, v253, 24
	s_waitcnt lgkmcnt(0)
	s_barrier

.Lxb_end_7:
	s_waitcnt vmcnt(0)
.LBB0_1037:
	s_or_b64 exec, exec, s[0:1]
	v_readlane_b32 s6, v253, 23
	v_readlane_b32 s7, v253, 24
	s_waitcnt lgkmcnt(0)
	s_barrier

.Lxb_end_8:
	s_waitcnt vmcnt(0)
.LBB0_1135:
	s_or_b64 exec, exec, s[0:1]
	v_readlane_b32 s6, v253, 23
	v_readlane_b32 s7, v253, 24
	s_waitcnt lgkmcnt(0)
	s_barrier

.Lxb_end_9:
	s_waitcnt vmcnt(0)
.LBB0_1211:
	s_or_b64 exec, exec, s[0:1]
	v_readlane_b32 s6, v253, 23
	v_readlane_b32 s7, v253, 24
	s_waitcnt lgkmcnt(0)
	s_barrier

.Lxb_end_10:
	s_waitcnt vmcnt(0)
.LBB0_1296:
	s_or_b64 exec, exec, s[0:1]
	v_readlane_b32 s6, v253, 23
	v_readlane_b32 s7, v253, 24
	s_waitcnt lgkmcnt(0)
	s_barrier

.Lxb_end_11:
	s_waitcnt vmcnt(0)
.LBB0_1369:
	s_or_b64 exec, exec, s[0:1]
	v_readlane_b32 s6, v253, 23
	v_readlane_b32 s7, v253, 24
	s_waitcnt lgkmcnt(0)
	s_barrier

.Lxb_end_12:
	s_waitcnt vmcnt(0)
.LBB0_1444:
	s_or_b64 exec, exec, s[0:1]
	v_readlane_b32 s6, v253, 23
	v_readlane_b32 s7, v253, 24
	s_waitcnt lgkmcnt(0)
	s_barrier

.Lxb_end_13:
	s_waitcnt vmcnt(0)
.LBB0_1561:
	s_or_b64 exec, exec, s[0:1]
	v_readlane_b32 s6, v253, 23
	v_readlane_b32 s7, v253, 24
	s_waitcnt lgkmcnt(0)
	s_barrier

.Lxb_end_14:
	s_waitcnt vmcnt(0)
.LBB0_1726:
	s_or_b64 exec, exec, s[0:1]
	v_readlane_b32 s6, v253, 23
	v_readlane_b32 s7, v253, 24
	s_waitcnt lgkmcnt(0)
	s_barrier

.Lxb_end_15:
	s_waitcnt vmcnt(0)
.LBB0_1860:
	s_or_b64 exec, exec, s[0:1]
	v_readlane_b32 s6, v253, 23
	v_readlane_b32 s7, v253, 24
	s_waitcnt lgkmcnt(0)
	s_barrier

.Lxb_end_16:
	s_waitcnt vmcnt(0)
.LBB0_1958:
	s_or_b64 exec, exec, s[0:1]
	v_readlane_b32 s6, v253, 23
	v_readlane_b32 s7, v253, 24
	s_waitcnt lgkmcnt(0)
	s_barrier

.Lxb_end_17:
	s_waitcnt vmcnt(0)
.LBB0_2037:
	s_or_b64 exec, exec, s[0:1]
	v_readlane_b32 s6, v253, 23
	v_readlane_b32 s7, v253, 24
	s_waitcnt lgkmcnt(0)
	s_barrier

.Lxb_end_18:
	s_waitcnt vmcnt(0)
.LBB0_2127:
	s_or_b64 exec, exec, s[0:1]
	v_readlane_b32 s6, v253, 23
	v_readlane_b32 s7, v253, 24
	s_waitcnt lgkmcnt(0)
	s_barrier

.Lxb_end_19:
	s_waitcnt vmcnt(0)
.LBB0_2202:
	s_or_b64 exec, exec, s[0:1]
	v_readlane_b32 s6, v253, 23
	v_readlane_b32 s7, v253, 24
	s_waitcnt lgkmcnt(0)
	s_barrier

.Lxb_end_20:
	s_waitcnt vmcnt(0)
.LBB0_2277:
	s_or_b64 exec, exec, s[0:1]
	v_readlane_b32 s6, v253, 23
	v_readlane_b32 s7, v253, 24
	s_waitcnt lgkmcnt(0)
	s_barrier

.Lxb_end_21:
	s_waitcnt vmcnt(0)
.LBB0_2352:
	s_or_b64 exec, exec, s[0:1]
	v_readlane_b32 s6, v253, 23
	v_readlane_b32 s7, v253, 24
	s_waitcnt lgkmcnt(0)
	s_barrier

.Lxb_end_22:
	s_waitcnt vmcnt(0)
.LBB0_2469:
	s_or_b64 exec, exec, s[0:1]
	v_readlane_b32 s6, v253, 23
	v_readlane_b32 s7, v253, 24
	s_waitcnt lgkmcnt(0)
	s_barrier

.Lxb_end_23:
	s_waitcnt vmcnt(0)
.LBB0_2634:
	s_or_b64 exec, exec, s[0:1]
	v_readlane_b32 s6, v253, 23
	v_readlane_b32 s7, v253, 24
	s_waitcnt lgkmcnt(0)
	s_barrier

.Lxb_end_24:
	s_waitcnt vmcnt(0)
.LBB0_2768:
	s_or_b64 exec, exec, s[0:1]
	v_readlane_b32 s6, v253, 23
	v_readlane_b32 s7, v253, 24
	s_waitcnt lgkmcnt(0)
	s_barrier

.Lxb_end_25:
	s_waitcnt vmcnt(0)
.LBB0_2866:
	s_or_b64 exec, exec, s[0:1]
	v_readlane_b32 s6, v253, 23
	v_readlane_b32 s7, v253, 24
	s_waitcnt lgkmcnt(0)
	s_barrier

.Lxb_end_26:
	s_waitcnt vmcnt(0)
.LBB0_2942:
	s_or_b64 exec, exec, s[0:1]
	v_readlane_b32 s6, v253, 23
	v_readlane_b32 s7, v253, 24
	s_waitcnt lgkmcnt(0)
	s_barrier

.Lxb_end_27:
	s_waitcnt vmcnt(0)
.LBB0_3009:
	s_or_b64 exec, exec, s[0:1]
	v_readlane_b32 s6, v253, 23
	v_readlane_b32 s7, v253, 24
	s_waitcnt lgkmcnt(0)
	s_barrier

.Lxb_end_28:
	s_waitcnt vmcnt(0)
.LBB0_3079:
	s_or_b64 exec, exec, s[0:1]
	v_readlane_b32 s6, v253, 23
	v_readlane_b32 s7, v253, 24
	s_waitcnt lgkmcnt(0)
	s_barrier

.Lxb_end_29:
	s_waitcnt vmcnt(0)
.LBB0_3170:
	s_or_b64 exec, exec, s[0:1]
	v_readlane_b32 s6, v253, 23
	v_readlane_b32 s7, v253, 24
	s_waitcnt lgkmcnt(0)
	s_barrier

.Lxb_end_30:
	s_waitcnt vmcnt(0)
.LBB0_3224:
	s_or_b64 exec, exec, s[0:1]
	v_readlane_b32 s6, v253, 23
	v_readlane_b32 s7, v253, 24
	s_waitcnt lgkmcnt(0)
	s_barrier

.Lxb_end_31:
	s_waitcnt vmcnt(0)
.LBB0_3299:
	s_or_b64 exec, exec, s[0:1]
	v_readlane_b32 s6, v253, 23
	v_readlane_b32 s7, v253, 24
	s_waitcnt lgkmcnt(0)
	s_barrier

.Lxb_end_32:
	s_waitcnt vmcnt(0)
.LBB0_3416:
	s_or_b64 exec, exec, s[0:1]
	v_readlane_b32 s6, v253, 23
	v_readlane_b32 s7, v253, 24
	s_waitcnt lgkmcnt(0)
	s_barrier

.Lxb_end_33:
	s_waitcnt vmcnt(0)
.LBB0_3597:
	s_or_b64 exec, exec, s[0:1]
	v_readlane_b32 s6, v253, 23
	v_readlane_b32 s7, v253, 24
	s_waitcnt lgkmcnt(0)
	s_barrier

.Lxb_end_34:
	s_waitcnt vmcnt(0)
.LBB0_3712:
	s_or_b64 exec, exec, s[0:1]
	v_readlane_b32 s6, v253, 23
	v_readlane_b32 s7, v253, 24
	s_waitcnt lgkmcnt(0)
	s_barrier

.Lxb_end_35:
	s_waitcnt vmcnt(0)
.LBB0_3791:
	s_or_b64 exec, exec, s[0:1]
	v_readlane_b32 s6, v253, 23
	v_readlane_b32 s7, v253, 24
	s_waitcnt lgkmcnt(0)
	s_barrier
